# phase 10 (U) rewritten as hand-scheduled f32 VALU dots on the V-phase skeleton (8 lanes per table row, DPP transposing butterfly), replaces the bf16-MFMA form
# speedup vs baseline: 1.0541x; 1.0216x over previous
.LBB0_1048:
	s_cmp_lt_i32 s40, 11
	s_cselect_b64 s[2:3], -1, 0
	s_cmp_gt_i32 s41, 10
	s_cselect_b64 s[4:5], -1, 0
	s_and_b64 s[10:11], s[2:3], s[4:5]
	s_andn2_b64 vcc, exec, s[10:11]
	s_cbranch_vccnz .LBB0_1075
	s_mov_b64 s[2:3], s[0:1]
	s_waitcnt vmcnt(0) lgkmcnt(0)
	v_mbcnt_lo_u32_b32 v0, -1, 0
	v_mbcnt_hi_u32_b32 v0, -1, v0
	s_load_dwordx2 s[4:5], s[2:3], 0xb8
	v_and_b32_e32 v9, 7, v0
	v_lshrrev_b32_e32 v10, 3, v0
	v_lshlrev_b32_e32 v1, 4, v9
	v_lshlrev_b32_e32 v2, 5, v10
	v_lshlrev_b32_e32 v3, 2, v0
	v_lshlrev_b32_e32 v4, 5, v9
	v_and_b32_e32 v12, 2, v0
	v_cmp_ne_u32_e64 s[44:45], 0, v12
	v_and_b32_e32 v12, 1, v0
	v_cmp_ne_u32_e64 s[42:43], 0, v12
	v_mov_b32_e32 v5, 0
	v_mov_b32_e32 v7, -1
	s_mov_b32 s47, 7
	s_mov_b32 s38, 0x200000
	s_mov_b32 s39, 0x20000
	s_lshl_b32 s16, s24, 1
	s_and_b32 s16, s16, 14
	s_mov_b32 s17, 0
	s_waitcnt lgkmcnt(0)
	s_add_u32 s28, s4, 0x18800000
	s_addc_u32 s29, s5, 0
.Lub_slice:
	s_lshl_b32 s2, s16, 8
	s_add_u32 s6, s4, s2
	s_addc_u32 s7, s5, 0
	s_add_u32 s6, s6, 0x121000
	s_addc_u32 s7, s7, 0
	s_add_u32 s30, s4, s2
	s_addc_u32 s31, s5, 0
	s_add_u32 s30, s30, 0x8000000
	s_addc_u32 s31, s31, 0
	s_lshl_b32 s2, s16, 22
	s_add_u32 s34, s4, s2
	s_addc_u32 s35, s5, 0
	s_add_u32 s34, s34, 0x10000000
	s_addc_u32 s35, s35, 0
	s_lshl_b32 s2, s16, 21
	s_add_u32 s36, s4, s2
	s_addc_u32 s37, s5, 0
	s_add_u32 s36, s36, 0x4000000
	s_addc_u32 s37, s37, 0
	s_and_b32 s37, s37, 0xffff
	s_mov_b64 exec, 1
	global_atomic_inc v6, v5, v7, s[6:7] sc0
	s_waitcnt vmcnt(0)
	v_readfirstlane_b32 s23, v6
	global_atomic_inc v6, v5, v7, s[6:7] sc0
	s_mov_b64 exec, -1
	s_mov_b32 s26, 0
	s_mov_b32 s27, 0
	s_cmp_lg_u32 s26, 32
	s_cbranch_scc1 .Lub_norot_p0
	v_readfirstlane_b32 s23, v6
	s_mov_b64 exec, 1
	global_atomic_inc v6, v5, v7, s[6:7] sc0
	s_mov_b64 exec, -1
	s_mov_b32 s26, 0

.Lub_got_p1:
	s_mov_b32 s21, s22
	s_mov_b32 s49, s50
	s_cmp_eq_u32 s48, 0
	s_cbranch_scc1 .Lub_next_slice
	s_lshl_b32 s2, s20, 8
	s_add_u32 s2, s28, s2
	s_addc_u32 s3, s29, 0
	global_load_dwordx4 v[8:11], v2, s[2:3]
	global_load_dwordx4 v[12:15], v2, s[2:3] offset:16
	s_lshl_b32 s2, s20, 12
	s_add_u32 s2, s30, s2
	s_addc_u32 s3, s31, 0
	global_load_dwordx4 v[24:27], v4, s[2:3]
	global_load_dwordx4 v[28:31], v4, s[2:3] offset:16
	s_lshl_b32 s2, s21, 8
	s_add_u32 s2, s28, s2
	s_addc_u32 s3, s29, 0
	global_load_dwordx4 v[16:19], v2, s[2:3]
	global_load_dwordx4 v[20:23], v2, s[2:3] offset:16
	s_waitcnt vmcnt(0)
	v_lshlrev_b32_sdwa v112, s47, v8 dst_sel:DWORD dst_unused:UNUSED_PAD src0_sel:DWORD src1_sel:WORD_0
	v_or_b32_e32 v112, v112, v1
	buffer_load_dwordx4 v[48:51], v112, s[36:39], 0 offen
	v_lshlrev_b32_sdwa v113, s47, v8 dst_sel:DWORD dst_unused:UNUSED_PAD src0_sel:DWORD src1_sel:WORD_1
	v_or_b32_e32 v113, v113, v1
	buffer_load_dwordx4 v[52:55], v113, s[36:39], 0 offen
	v_lshlrev_b32_sdwa v112, s47, v9 dst_sel:DWORD dst_unused:UNUSED_PAD src0_sel:DWORD src1_sel:WORD_0
	v_or_b32_e32 v112, v112, v1
	buffer_load_dwordx4 v[56:59], v112, s[36:39], 0 offen
	v_lshlrev_b32_sdwa v113, s47, v9 dst_sel:DWORD dst_unused:UNUSED_PAD src0_sel:DWORD src1_sel:WORD_1
	v_or_b32_e32 v113, v113, v1
	buffer_load_dwordx4 v[60:63], v113, s[36:39], 0 offen
	v_lshlrev_b32_sdwa v112, s47, v10 dst_sel:DWORD dst_unused:UNUSED_PAD src0_sel:DWORD src1_sel:WORD_0
	v_or_b32_e32 v112, v112, v1
	buffer_load_dwordx4 v[64:67], v112, s[36:39], 0 offen
	v_lshlrev_b32_sdwa v113, s47, v10 dst_sel:DWORD dst_unused:UNUSED_PAD src0_sel:DWORD src1_sel:WORD_1
	v_or_b32_e32 v113, v113, v1
	buffer_load_dwordx4 v[68:71], v113, s[36:39], 0 offen
	v_lshlrev_b32_sdwa v112, s47, v11 dst_sel:DWORD dst_unused:UNUSED_PAD src0_sel:DWORD src1_sel:WORD_0
	v_or_b32_e32 v112, v112, v1
	buffer_load_dwordx4 v[72:75], v112, s[36:39], 0 offen
	v_lshlrev_b32_sdwa v113, s47, v11 dst_sel:DWORD dst_unused:UNUSED_PAD src0_sel:DWORD src1_sel:WORD_1
	v_or_b32_e32 v113, v113, v1
	buffer_load_dwordx4 v[76:79], v113, s[36:39], 0 offen
	v_lshlrev_b32_sdwa v112, s47, v12 dst_sel:DWORD dst_unused:UNUSED_PAD src0_sel:DWORD src1_sel:WORD_0
	v_or_b32_e32 v112, v112, v1
	buffer_load_dwordx4 v[80:83], v112, s[36:39], 0 offen
	v_lshlrev_b32_sdwa v113, s47, v12 dst_sel:DWORD dst_unused:UNUSED_PAD src0_sel:DWORD src1_sel:WORD_1
	v_or_b32_e32 v113, v113, v1
	buffer_load_dwordx4 v[84:87], v113, s[36:39], 0 offen
	v_lshlrev_b32_sdwa v112, s47, v13 dst_sel:DWORD dst_unused:UNUSED_PAD src0_sel:DWORD src1_sel:WORD_0
	v_or_b32_e32 v112, v112, v1
	buffer_load_dwordx4 v[88:91], v112, s[36:39], 0 offen
	v_lshlrev_b32_sdwa v113, s47, v13 dst_sel:DWORD dst_unused:UNUSED_PAD src0_sel:DWORD src1_sel:WORD_1
	v_or_b32_e32 v113, v113, v1
	buffer_load_dwordx4 v[92:95], v113, s[36:39], 0 offen
	v_lshlrev_b32_sdwa v112, s47, v14 dst_sel:DWORD dst_unused:UNUSED_PAD src0_sel:DWORD src1_sel:WORD_0
	v_or_b32_e32 v112, v112, v1
	buffer_load_dwordx4 v[96:99], v112, s[36:39], 0 offen
	v_lshlrev_b32_sdwa v113, s47, v14 dst_sel:DWORD dst_unused:UNUSED_PAD src0_sel:DWORD src1_sel:WORD_1
	v_or_b32_e32 v113, v113, v1
	buffer_load_dwordx4 v[100:103], v113, s[36:39], 0 offen
	v_lshlrev_b32_sdwa v112, s47, v15 dst_sel:DWORD dst_unused:UNUSED_PAD src0_sel:DWORD src1_sel:WORD_0
	v_or_b32_e32 v112, v112, v1
	buffer_load_dwordx4 v[104:107], v112, s[36:39], 0 offen
	v_lshlrev_b32_sdwa v113, s47, v15 dst_sel:DWORD dst_unused:UNUSED_PAD src0_sel:DWORD src1_sel:WORD_1
	v_or_b32_e32 v113, v113, v1
	buffer_load_dwordx4 v[108:111], v113, s[36:39], 0 offen
	global_load_dword v252, v5, s[28:29]

.Lub_got_l0:
	s_lshl_b32 s2, s22, 8
	s_add_u32 s2, s28, s2
	s_addc_u32 s3, s29, 0
	global_load_dwordx4 v[8:11], v2, s[2:3]
	global_load_dwordx4 v[12:15], v2, s[2:3] offset:16
	s_lshl_b32 s2, s21, 12
	s_add_u32 s2, s30, s2
	s_addc_u32 s3, s31, 0
	global_load_dwordx4 v[32:35], v4, s[2:3]
	global_load_dwordx4 v[36:39], v4, s[2:3] offset:16
	s_waitcnt vmcnt(20)
	v_cvt_pk_f32_fp8_e32 v[116:117], v48
	v_cvt_pk_f32_fp8_sdwa v[118:119], v48 src0_sel:WORD_1
	v_cvt_pk_f32_fp8_e32 v[120:121], v49
	v_cvt_pk_f32_fp8_sdwa v[122:123], v49 src0_sel:WORD_1
	v_cvt_pk_f32_fp8_e32 v[124:125], v50
	v_cvt_pk_f32_fp8_sdwa v[126:127], v50 src0_sel:WORD_1
	v_cvt_pk_f32_fp8_e32 v[128:129], v51
	v_cvt_pk_f32_fp8_sdwa v[130:131], v51 src0_sel:WORD_1
	v_lshlrev_b32_e32 v148, 16, v24
	v_and_b32_e32 v149, 0xffff0000, v24
	v_lshlrev_b32_e32 v150, 16, v25
	v_and_b32_e32 v151, 0xffff0000, v25
	v_lshlrev_b32_e32 v152, 16, v26
	v_and_b32_e32 v153, 0xffff0000, v26
	v_lshlrev_b32_e32 v154, 16, v27
	v_and_b32_e32 v155, 0xffff0000, v27
	v_lshlrev_b32_e32 v156, 16, v28
	v_and_b32_e32 v157, 0xffff0000, v28
	v_lshlrev_b32_e32 v158, 16, v29
	v_and_b32_e32 v159, 0xffff0000, v29
	v_lshlrev_b32_e32 v160, 16, v30
	v_and_b32_e32 v161, 0xffff0000, v30
	v_lshlrev_b32_e32 v162, 16, v31
	v_and_b32_e32 v163, 0xffff0000, v31
	v_lshlrev_b32_sdwa v112, s47, v16 dst_sel:DWORD dst_unused:UNUSED_PAD src0_sel:DWORD src1_sel:WORD_0
	v_or_b32_e32 v112, v112, v1
	buffer_load_dwordx4 v[48:51], v112, s[36:39], 0 offen
	v_pk_mul_f32 v[164:165], v[116:117], v[148:149]
	v_pk_fma_f32 v[164:165], v[118:119], v[150:151], v[164:165]
	v_pk_fma_f32 v[164:165], v[120:121], v[152:153], v[164:165]
	v_pk_fma_f32 v[164:165], v[122:123], v[154:155], v[164:165]
	v_pk_fma_f32 v[164:165], v[124:125], v[156:157], v[164:165]
	v_pk_fma_f32 v[164:165], v[126:127], v[158:159], v[164:165]
	v_pk_fma_f32 v[164:165], v[128:129], v[160:161], v[164:165]
	v_pk_fma_f32 v[164:165], v[130:131], v[162:163], v[164:165]
	v_add_f32_e32 v168, v164, v165
	s_waitcnt vmcnt(20)
	v_cvt_pk_f32_fp8_e32 v[132:133], v52
	v_cvt_pk_f32_fp8_sdwa v[134:135], v52 src0_sel:WORD_1
	v_cvt_pk_f32_fp8_e32 v[136:137], v53
	v_cvt_pk_f32_fp8_sdwa v[138:139], v53 src0_sel:WORD_1
	v_cvt_pk_f32_fp8_e32 v[140:141], v54
	v_cvt_pk_f32_fp8_sdwa v[142:143], v54 src0_sel:WORD_1
	v_cvt_pk_f32_fp8_e32 v[144:145], v55
	v_cvt_pk_f32_fp8_sdwa v[146:147], v55 src0_sel:WORD_1
	v_lshlrev_b32_sdwa v113, s47, v16 dst_sel:DWORD dst_unused:UNUSED_PAD src0_sel:DWORD src1_sel:WORD_1
	v_or_b32_e32 v113, v113, v1
	buffer_load_dwordx4 v[52:55], v113, s[36:39], 0 offen
	v_pk_mul_f32 v[166:167], v[132:133], v[148:149]
	v_pk_fma_f32 v[166:167], v[134:135], v[150:151], v[166:167]
	v_pk_fma_f32 v[166:167], v[136:137], v[152:153], v[166:167]
	v_pk_fma_f32 v[166:167], v[138:139], v[154:155], v[166:167]
	v_pk_fma_f32 v[166:167], v[140:141], v[156:157], v[166:167]
	v_pk_fma_f32 v[166:167], v[142:143], v[158:159], v[166:167]
	v_pk_fma_f32 v[166:167], v[144:145], v[160:161], v[166:167]
	v_pk_fma_f32 v[166:167], v[146:147], v[162:163], v[166:167]
	v_add_f32_e32 v169, v166, v167
	s_waitcnt vmcnt(20)
	v_cvt_pk_f32_fp8_e32 v[116:117], v56
	v_cvt_pk_f32_fp8_sdwa v[118:119], v56 src0_sel:WORD_1
	v_cvt_pk_f32_fp8_e32 v[120:121], v57
	v_cvt_pk_f32_fp8_sdwa v[122:123], v57 src0_sel:WORD_1
	v_cvt_pk_f32_fp8_e32 v[124:125], v58
	v_cvt_pk_f32_fp8_sdwa v[126:127], v58 src0_sel:WORD_1
	v_cvt_pk_f32_fp8_e32 v[128:129], v59
	v_cvt_pk_f32_fp8_sdwa v[130:131], v59 src0_sel:WORD_1
	v_lshlrev_b32_sdwa v112, s47, v17 dst_sel:DWORD dst_unused:UNUSED_PAD src0_sel:DWORD src1_sel:WORD_0
	v_or_b32_e32 v112, v112, v1
	buffer_load_dwordx4 v[56:59], v112, s[36:39], 0 offen
	v_pk_mul_f32 v[164:165], v[116:117], v[148:149]
	v_pk_fma_f32 v[164:165], v[118:119], v[150:151], v[164:165]
	v_pk_fma_f32 v[164:165], v[120:121], v[152:153], v[164:165]
	v_pk_fma_f32 v[164:165], v[122:123], v[154:155], v[164:165]
	v_pk_fma_f32 v[164:165], v[124:125], v[156:157], v[164:165]
	v_pk_fma_f32 v[164:165], v[126:127], v[158:159], v[164:165]
	v_pk_fma_f32 v[164:165], v[128:129], v[160:161], v[164:165]
	v_pk_fma_f32 v[164:165], v[130:131], v[162:163], v[164:165]
	v_add_f32_e32 v170, v164, v165
	s_waitcnt vmcnt(20)
	v_cvt_pk_f32_fp8_e32 v[132:133], v60
	v_cvt_pk_f32_fp8_sdwa v[134:135], v60 src0_sel:WORD_1
	v_cvt_pk_f32_fp8_e32 v[136:137], v61
	v_cvt_pk_f32_fp8_sdwa v[138:139], v61 src0_sel:WORD_1
	v_cvt_pk_f32_fp8_e32 v[140:141], v62
	v_cvt_pk_f32_fp8_sdwa v[142:143], v62 src0_sel:WORD_1
	v_cvt_pk_f32_fp8_e32 v[144:145], v63
	v_cvt_pk_f32_fp8_sdwa v[146:147], v63 src0_sel:WORD_1
	v_lshlrev_b32_sdwa v113, s47, v17 dst_sel:DWORD dst_unused:UNUSED_PAD src0_sel:DWORD src1_sel:WORD_1
	v_or_b32_e32 v113, v113, v1
	buffer_load_dwordx4 v[60:63], v113, s[36:39], 0 offen
	v_pk_mul_f32 v[166:167], v[132:133], v[148:149]
	v_pk_fma_f32 v[166:167], v[134:135], v[150:151], v[166:167]
	v_pk_fma_f32 v[166:167], v[136:137], v[152:153], v[166:167]
	v_pk_fma_f32 v[166:167], v[138:139], v[154:155], v[166:167]
	v_pk_fma_f32 v[166:167], v[140:141], v[156:157], v[166:167]
	v_pk_fma_f32 v[166:167], v[142:143], v[158:159], v[166:167]
	v_pk_fma_f32 v[166:167], v[144:145], v[160:161], v[166:167]
	v_pk_fma_f32 v[166:167], v[146:147], v[162:163], v[166:167]
	v_add_f32_e32 v171, v166, v167
	s_waitcnt vmcnt(20)
	v_cvt_pk_f32_fp8_e32 v[116:117], v64
	v_cvt_pk_f32_fp8_sdwa v[118:119], v64 src0_sel:WORD_1
	v_cvt_pk_f32_fp8_e32 v[120:121], v65
	v_cvt_pk_f32_fp8_sdwa v[122:123], v65 src0_sel:WORD_1
	v_cvt_pk_f32_fp8_e32 v[124:125], v66
	v_cvt_pk_f32_fp8_sdwa v[126:127], v66 src0_sel:WORD_1
	v_cvt_pk_f32_fp8_e32 v[128:129], v67
	v_cvt_pk_f32_fp8_sdwa v[130:131], v67 src0_sel:WORD_1
	v_lshlrev_b32_sdwa v112, s47, v18 dst_sel:DWORD dst_unused:UNUSED_PAD src0_sel:DWORD src1_sel:WORD_0
	v_or_b32_e32 v112, v112, v1
	buffer_load_dwordx4 v[64:67], v112, s[36:39], 0 offen
	v_pk_mul_f32 v[164:165], v[116:117], v[148:149]
	v_pk_fma_f32 v[164:165], v[118:119], v[150:151], v[164:165]
	v_pk_fma_f32 v[164:165], v[120:121], v[152:153], v[164:165]
	v_pk_fma_f32 v[164:165], v[122:123], v[154:155], v[164:165]
	v_pk_fma_f32 v[164:165], v[124:125], v[156:157], v[164:165]
	v_pk_fma_f32 v[164:165], v[126:127], v[158:159], v[164:165]
	v_pk_fma_f32 v[164:165], v[128:129], v[160:161], v[164:165]
	v_pk_fma_f32 v[164:165], v[130:131], v[162:163], v[164:165]
	v_add_f32_e32 v172, v164, v165
	s_waitcnt vmcnt(20)
	v_cvt_pk_f32_fp8_e32 v[132:133], v68
	v_cvt_pk_f32_fp8_sdwa v[134:135], v68 src0_sel:WORD_1
	v_cvt_pk_f32_fp8_e32 v[136:137], v69
	v_cvt_pk_f32_fp8_sdwa v[138:139], v69 src0_sel:WORD_1
	v_cvt_pk_f32_fp8_e32 v[140:141], v70
	v_cvt_pk_f32_fp8_sdwa v[142:143], v70 src0_sel:WORD_1
	v_cvt_pk_f32_fp8_e32 v[144:145], v71
	v_cvt_pk_f32_fp8_sdwa v[146:147], v71 src0_sel:WORD_1
	v_lshlrev_b32_sdwa v113, s47, v18 dst_sel:DWORD dst_unused:UNUSED_PAD src0_sel:DWORD src1_sel:WORD_1
	v_or_b32_e32 v113, v113, v1
	buffer_load_dwordx4 v[68:71], v113, s[36:39], 0 offen
	v_pk_mul_f32 v[166:167], v[132:133], v[148:149]
	v_pk_fma_f32 v[166:167], v[134:135], v[150:151], v[166:167]
	v_pk_fma_f32 v[166:167], v[136:137], v[152:153], v[166:167]
	v_pk_fma_f32 v[166:167], v[138:139], v[154:155], v[166:167]
	v_pk_fma_f32 v[166:167], v[140:141], v[156:157], v[166:167]
	v_pk_fma_f32 v[166:167], v[142:143], v[158:159], v[166:167]
	v_pk_fma_f32 v[166:167], v[144:145], v[160:161], v[166:167]
	v_pk_fma_f32 v[166:167], v[146:147], v[162:163], v[166:167]
	v_add_f32_e32 v173, v166, v167
	s_waitcnt vmcnt(20)
	v_cvt_pk_f32_fp8_e32 v[116:117], v72
	v_cvt_pk_f32_fp8_sdwa v[118:119], v72 src0_sel:WORD_1
	v_cvt_pk_f32_fp8_e32 v[120:121], v73
	v_cvt_pk_f32_fp8_sdwa v[122:123], v73 src0_sel:WORD_1
	v_cvt_pk_f32_fp8_e32 v[124:125], v74
	v_cvt_pk_f32_fp8_sdwa v[126:127], v74 src0_sel:WORD_1
	v_cvt_pk_f32_fp8_e32 v[128:129], v75
	v_cvt_pk_f32_fp8_sdwa v[130:131], v75 src0_sel:WORD_1
	v_lshlrev_b32_sdwa v112, s47, v19 dst_sel:DWORD dst_unused:UNUSED_PAD src0_sel:DWORD src1_sel:WORD_0
	v_or_b32_e32 v112, v112, v1
	buffer_load_dwordx4 v[72:75], v112, s[36:39], 0 offen
	v_pk_mul_f32 v[164:165], v[116:117], v[148:149]
	v_pk_fma_f32 v[164:165], v[118:119], v[150:151], v[164:165]
	v_pk_fma_f32 v[164:165], v[120:121], v[152:153], v[164:165]
	v_pk_fma_f32 v[164:165], v[122:123], v[154:155], v[164:165]
	v_pk_fma_f32 v[164:165], v[124:125], v[156:157], v[164:165]
	v_pk_fma_f32 v[164:165], v[126:127], v[158:159], v[164:165]
	v_pk_fma_f32 v[164:165], v[128:129], v[160:161], v[164:165]
	v_pk_fma_f32 v[164:165], v[130:131], v[162:163], v[164:165]
	v_add_f32_e32 v174, v164, v165
	s_waitcnt vmcnt(20)
	v_cvt_pk_f32_fp8_e32 v[132:133], v76
	v_cvt_pk_f32_fp8_sdwa v[134:135], v76 src0_sel:WORD_1
	v_cvt_pk_f32_fp8_e32 v[136:137], v77
	v_cvt_pk_f32_fp8_sdwa v[138:139], v77 src0_sel:WORD_1
	v_cvt_pk_f32_fp8_e32 v[140:141], v78
	v_cvt_pk_f32_fp8_sdwa v[142:143], v78 src0_sel:WORD_1
	v_cvt_pk_f32_fp8_e32 v[144:145], v79
	v_cvt_pk_f32_fp8_sdwa v[146:147], v79 src0_sel:WORD_1
	v_lshlrev_b32_sdwa v113, s47, v19 dst_sel:DWORD dst_unused:UNUSED_PAD src0_sel:DWORD src1_sel:WORD_1
	v_or_b32_e32 v113, v113, v1
	buffer_load_dwordx4 v[76:79], v113, s[36:39], 0 offen
	v_pk_mul_f32 v[166:167], v[132:133], v[148:149]
	v_pk_fma_f32 v[166:167], v[134:135], v[150:151], v[166:167]
	v_pk_fma_f32 v[166:167], v[136:137], v[152:153], v[166:167]
	v_pk_fma_f32 v[166:167], v[138:139], v[154:155], v[166:167]
	v_pk_fma_f32 v[166:167], v[140:141], v[156:157], v[166:167]
	v_pk_fma_f32 v[166:167], v[142:143], v[158:159], v[166:167]
	v_pk_fma_f32 v[166:167], v[144:145], v[160:161], v[166:167]
	v_pk_fma_f32 v[166:167], v[146:147], v[162:163], v[166:167]
	v_add_f32_e32 v175, v166, v167
	s_waitcnt vmcnt(20)
	v_cvt_pk_f32_fp8_e32 v[116:117], v80
	v_cvt_pk_f32_fp8_sdwa v[118:119], v80 src0_sel:WORD_1
	v_cvt_pk_f32_fp8_e32 v[120:121], v81
	v_cvt_pk_f32_fp8_sdwa v[122:123], v81 src0_sel:WORD_1
	v_cvt_pk_f32_fp8_e32 v[124:125], v82
	v_cvt_pk_f32_fp8_sdwa v[126:127], v82 src0_sel:WORD_1
	v_cvt_pk_f32_fp8_e32 v[128:129], v83
	v_cvt_pk_f32_fp8_sdwa v[130:131], v83 src0_sel:WORD_1
	v_lshlrev_b32_sdwa v112, s47, v20 dst_sel:DWORD dst_unused:UNUSED_PAD src0_sel:DWORD src1_sel:WORD_0
	v_or_b32_e32 v112, v112, v1
	buffer_load_dwordx4 v[80:83], v112, s[36:39], 0 offen
	v_pk_mul_f32 v[164:165], v[116:117], v[148:149]
	v_pk_fma_f32 v[164:165], v[118:119], v[150:151], v[164:165]
	v_pk_fma_f32 v[164:165], v[120:121], v[152:153], v[164:165]
	v_pk_fma_f32 v[164:165], v[122:123], v[154:155], v[164:165]
	v_pk_fma_f32 v[164:165], v[124:125], v[156:157], v[164:165]
	v_pk_fma_f32 v[164:165], v[126:127], v[158:159], v[164:165]
	v_pk_fma_f32 v[164:165], v[128:129], v[160:161], v[164:165]
	v_pk_fma_f32 v[164:165], v[130:131], v[162:163], v[164:165]
	v_add_f32_e32 v176, v164, v165
	s_waitcnt vmcnt(20)
	v_cvt_pk_f32_fp8_e32 v[132:133], v84
	v_cvt_pk_f32_fp8_sdwa v[134:135], v84 src0_sel:WORD_1
	v_cvt_pk_f32_fp8_e32 v[136:137], v85
	v_cvt_pk_f32_fp8_sdwa v[138:139], v85 src0_sel:WORD_1
	v_cvt_pk_f32_fp8_e32 v[140:141], v86
	v_cvt_pk_f32_fp8_sdwa v[142:143], v86 src0_sel:WORD_1
	v_cvt_pk_f32_fp8_e32 v[144:145], v87
	v_cvt_pk_f32_fp8_sdwa v[146:147], v87 src0_sel:WORD_1
	v_lshlrev_b32_sdwa v113, s47, v20 dst_sel:DWORD dst_unused:UNUSED_PAD src0_sel:DWORD src1_sel:WORD_1
	v_or_b32_e32 v113, v113, v1
	buffer_load_dwordx4 v[84:87], v113, s[36:39], 0 offen
	v_pk_mul_f32 v[166:167], v[132:133], v[148:149]
	v_pk_fma_f32 v[166:167], v[134:135], v[150:151], v[166:167]
	v_pk_fma_f32 v[166:167], v[136:137], v[152:153], v[166:167]
	v_pk_fma_f32 v[166:167], v[138:139], v[154:155], v[166:167]
	v_pk_fma_f32 v[166:167], v[140:141], v[156:157], v[166:167]
	v_pk_fma_f32 v[166:167], v[142:143], v[158:159], v[166:167]
	v_pk_fma_f32 v[166:167], v[144:145], v[160:161], v[166:167]
	v_pk_fma_f32 v[166:167], v[146:147], v[162:163], v[166:167]
	v_add_f32_e32 v177, v166, v167
	s_waitcnt vmcnt(20)
	v_cvt_pk_f32_fp8_e32 v[116:117], v88
	v_cvt_pk_f32_fp8_sdwa v[118:119], v88 src0_sel:WORD_1
	v_cvt_pk_f32_fp8_e32 v[120:121], v89
	v_cvt_pk_f32_fp8_sdwa v[122:123], v89 src0_sel:WORD_1
	v_cvt_pk_f32_fp8_e32 v[124:125], v90
	v_cvt_pk_f32_fp8_sdwa v[126:127], v90 src0_sel:WORD_1
	v_cvt_pk_f32_fp8_e32 v[128:129], v91
	v_cvt_pk_f32_fp8_sdwa v[130:131], v91 src0_sel:WORD_1
	v_lshlrev_b32_sdwa v112, s47, v21 dst_sel:DWORD dst_unused:UNUSED_PAD src0_sel:DWORD src1_sel:WORD_0
	v_or_b32_e32 v112, v112, v1
	buffer_load_dwordx4 v[88:91], v112, s[36:39], 0 offen
	v_pk_mul_f32 v[164:165], v[116:117], v[148:149]
	v_pk_fma_f32 v[164:165], v[118:119], v[150:151], v[164:165]
	v_pk_fma_f32 v[164:165], v[120:121], v[152:153], v[164:165]
	v_pk_fma_f32 v[164:165], v[122:123], v[154:155], v[164:165]
	v_pk_fma_f32 v[164:165], v[124:125], v[156:157], v[164:165]
	v_pk_fma_f32 v[164:165], v[126:127], v[158:159], v[164:165]
	v_pk_fma_f32 v[164:165], v[128:129], v[160:161], v[164:165]
	v_pk_fma_f32 v[164:165], v[130:131], v[162:163], v[164:165]
	v_add_f32_e32 v178, v164, v165
	s_waitcnt vmcnt(20)
	v_cvt_pk_f32_fp8_e32 v[132:133], v92
	v_cvt_pk_f32_fp8_sdwa v[134:135], v92 src0_sel:WORD_1
	v_cvt_pk_f32_fp8_e32 v[136:137], v93
	v_cvt_pk_f32_fp8_sdwa v[138:139], v93 src0_sel:WORD_1
	v_cvt_pk_f32_fp8_e32 v[140:141], v94
	v_cvt_pk_f32_fp8_sdwa v[142:143], v94 src0_sel:WORD_1
	v_cvt_pk_f32_fp8_e32 v[144:145], v95
	v_cvt_pk_f32_fp8_sdwa v[146:147], v95 src0_sel:WORD_1
	v_lshlrev_b32_sdwa v113, s47, v21 dst_sel:DWORD dst_unused:UNUSED_PAD src0_sel:DWORD src1_sel:WORD_1
	v_or_b32_e32 v113, v113, v1
	buffer_load_dwordx4 v[92:95], v113, s[36:39], 0 offen
	v_pk_mul_f32 v[166:167], v[132:133], v[148:149]
	v_pk_fma_f32 v[166:167], v[134:135], v[150:151], v[166:167]
	v_pk_fma_f32 v[166:167], v[136:137], v[152:153], v[166:167]
	v_pk_fma_f32 v[166:167], v[138:139], v[154:155], v[166:167]
	v_pk_fma_f32 v[166:167], v[140:141], v[156:157], v[166:167]
	v_pk_fma_f32 v[166:167], v[142:143], v[158:159], v[166:167]
	v_pk_fma_f32 v[166:167], v[144:145], v[160:161], v[166:167]
	v_pk_fma_f32 v[166:167], v[146:147], v[162:163], v[166:167]
	v_add_f32_e32 v179, v166, v167
	s_waitcnt vmcnt(20)
	v_cvt_pk_f32_fp8_e32 v[116:117], v96
	v_cvt_pk_f32_fp8_sdwa v[118:119], v96 src0_sel:WORD_1
	v_cvt_pk_f32_fp8_e32 v[120:121], v97
	v_cvt_pk_f32_fp8_sdwa v[122:123], v97 src0_sel:WORD_1
	v_cvt_pk_f32_fp8_e32 v[124:125], v98
	v_cvt_pk_f32_fp8_sdwa v[126:127], v98 src0_sel:WORD_1
	v_cvt_pk_f32_fp8_e32 v[128:129], v99
	v_cvt_pk_f32_fp8_sdwa v[130:131], v99 src0_sel:WORD_1
	v_lshlrev_b32_sdwa v112, s47, v22 dst_sel:DWORD dst_unused:UNUSED_PAD src0_sel:DWORD src1_sel:WORD_0
	v_or_b32_e32 v112, v112, v1
	buffer_load_dwordx4 v[96:99], v112, s[36:39], 0 offen
	v_pk_mul_f32 v[164:165], v[116:117], v[148:149]
	v_pk_fma_f32 v[164:165], v[118:119], v[150:151], v[164:165]
	v_pk_fma_f32 v[164:165], v[120:121], v[152:153], v[164:165]
	v_pk_fma_f32 v[164:165], v[122:123], v[154:155], v[164:165]
	v_pk_fma_f32 v[164:165], v[124:125], v[156:157], v[164:165]
	v_pk_fma_f32 v[164:165], v[126:127], v[158:159], v[164:165]
	v_pk_fma_f32 v[164:165], v[128:129], v[160:161], v[164:165]
	v_pk_fma_f32 v[164:165], v[130:131], v[162:163], v[164:165]
	v_add_f32_e32 v180, v164, v165
	s_waitcnt vmcnt(20)
	v_cvt_pk_f32_fp8_e32 v[132:133], v100
	v_cvt_pk_f32_fp8_sdwa v[134:135], v100 src0_sel:WORD_1
	v_cvt_pk_f32_fp8_e32 v[136:137], v101
	v_cvt_pk_f32_fp8_sdwa v[138:139], v101 src0_sel:WORD_1
	v_cvt_pk_f32_fp8_e32 v[140:141], v102
	v_cvt_pk_f32_fp8_sdwa v[142:143], v102 src0_sel:WORD_1
	v_cvt_pk_f32_fp8_e32 v[144:145], v103
	v_cvt_pk_f32_fp8_sdwa v[146:147], v103 src0_sel:WORD_1
	v_lshlrev_b32_sdwa v113, s47, v22 dst_sel:DWORD dst_unused:UNUSED_PAD src0_sel:DWORD src1_sel:WORD_1
	v_or_b32_e32 v113, v113, v1
	buffer_load_dwordx4 v[100:103], v113, s[36:39], 0 offen
	v_pk_mul_f32 v[166:167], v[132:133], v[148:149]
	v_pk_fma_f32 v[166:167], v[134:135], v[150:151], v[166:167]
	v_pk_fma_f32 v[166:167], v[136:137], v[152:153], v[166:167]
	v_pk_fma_f32 v[166:167], v[138:139], v[154:155], v[166:167]
	v_pk_fma_f32 v[166:167], v[140:141], v[156:157], v[166:167]
	v_pk_fma_f32 v[166:167], v[142:143], v[158:159], v[166:167]
	v_pk_fma_f32 v[166:167], v[144:145], v[160:161], v[166:167]
	v_pk_fma_f32 v[166:167], v[146:147], v[162:163], v[166:167]
	v_add_f32_e32 v181, v166, v167
	s_waitcnt vmcnt(20)
	v_cvt_pk_f32_fp8_e32 v[116:117], v104
	v_cvt_pk_f32_fp8_sdwa v[118:119], v104 src0_sel:WORD_1
	v_cvt_pk_f32_fp8_e32 v[120:121], v105
	v_cvt_pk_f32_fp8_sdwa v[122:123], v105 src0_sel:WORD_1
	v_cvt_pk_f32_fp8_e32 v[124:125], v106
	v_cvt_pk_f32_fp8_sdwa v[126:127], v106 src0_sel:WORD_1
	v_cvt_pk_f32_fp8_e32 v[128:129], v107
	v_cvt_pk_f32_fp8_sdwa v[130:131], v107 src0_sel:WORD_1
	v_lshlrev_b32_sdwa v112, s47, v23 dst_sel:DWORD dst_unused:UNUSED_PAD src0_sel:DWORD src1_sel:WORD_0
	v_or_b32_e32 v112, v112, v1
	buffer_load_dwordx4 v[104:107], v112, s[36:39], 0 offen
	v_pk_mul_f32 v[164:165], v[116:117], v[148:149]
	v_pk_fma_f32 v[164:165], v[118:119], v[150:151], v[164:165]
	v_pk_fma_f32 v[164:165], v[120:121], v[152:153], v[164:165]
	v_pk_fma_f32 v[164:165], v[122:123], v[154:155], v[164:165]
	v_pk_fma_f32 v[164:165], v[124:125], v[156:157], v[164:165]
	v_pk_fma_f32 v[164:165], v[126:127], v[158:159], v[164:165]
	v_pk_fma_f32 v[164:165], v[128:129], v[160:161], v[164:165]
	v_pk_fma_f32 v[164:165], v[130:131], v[162:163], v[164:165]
	v_add_f32_e32 v182, v164, v165
	s_waitcnt vmcnt(20)
	v_cvt_pk_f32_fp8_e32 v[132:133], v108
	v_cvt_pk_f32_fp8_sdwa v[134:135], v108 src0_sel:WORD_1
	v_cvt_pk_f32_fp8_e32 v[136:137], v109
	v_cvt_pk_f32_fp8_sdwa v[138:139], v109 src0_sel:WORD_1
	v_cvt_pk_f32_fp8_e32 v[140:141], v110
	v_cvt_pk_f32_fp8_sdwa v[142:143], v110 src0_sel:WORD_1
	v_cvt_pk_f32_fp8_e32 v[144:145], v111
	v_cvt_pk_f32_fp8_sdwa v[146:147], v111 src0_sel:WORD_1
	v_lshlrev_b32_sdwa v113, s47, v23 dst_sel:DWORD dst_unused:UNUSED_PAD src0_sel:DWORD src1_sel:WORD_1
	v_or_b32_e32 v113, v113, v1
	buffer_load_dwordx4 v[108:111], v113, s[36:39], 0 offen
	v_pk_mul_f32 v[166:167], v[132:133], v[148:149]
	v_pk_fma_f32 v[166:167], v[134:135], v[150:151], v[166:167]
	v_pk_fma_f32 v[166:167], v[136:137], v[152:153], v[166:167]
	v_pk_fma_f32 v[166:167], v[138:139], v[154:155], v[166:167]
	v_pk_fma_f32 v[166:167], v[140:141], v[156:157], v[166:167]
	v_pk_fma_f32 v[166:167], v[142:143], v[158:159], v[166:167]
	v_pk_fma_f32 v[166:167], v[144:145], v[160:161], v[166:167]
	v_pk_fma_f32 v[166:167], v[146:147], v[162:163], v[166:167]
	v_add_f32_e32 v183, v166, v167
	s_nop 1
	v_add_f32_dpp v184, v168, v168 row_half_mirror row_mask:0xf bank_mask:0x5
	v_add_f32_dpp v184, v176, v176 row_half_mirror row_mask:0xf bank_mask:0xa
	v_add_f32_dpp v185, v169, v169 row_half_mirror row_mask:0xf bank_mask:0x5
	v_add_f32_dpp v185, v177, v177 row_half_mirror row_mask:0xf bank_mask:0xa
	v_add_f32_dpp v186, v170, v170 row_half_mirror row_mask:0xf bank_mask:0x5
	v_add_f32_dpp v186, v178, v178 row_half_mirror row_mask:0xf bank_mask:0xa
	v_add_f32_dpp v187, v171, v171 row_half_mirror row_mask:0xf bank_mask:0x5
	v_add_f32_dpp v187, v179, v179 row_half_mirror row_mask:0xf bank_mask:0xa
	v_add_f32_dpp v188, v172, v172 row_half_mirror row_mask:0xf bank_mask:0x5
	v_add_f32_dpp v188, v180, v180 row_half_mirror row_mask:0xf bank_mask:0xa
	v_add_f32_dpp v189, v173, v173 row_half_mirror row_mask:0xf bank_mask:0x5
	v_add_f32_dpp v189, v181, v181 row_half_mirror row_mask:0xf bank_mask:0xa
	v_add_f32_dpp v190, v174, v174 row_half_mirror row_mask:0xf bank_mask:0x5
	v_add_f32_dpp v190, v182, v182 row_half_mirror row_mask:0xf bank_mask:0xa
	v_add_f32_dpp v191, v175, v175 row_half_mirror row_mask:0xf bank_mask:0x5
	v_add_f32_dpp v191, v183, v183 row_half_mirror row_mask:0xf bank_mask:0xa
	v_cndmask_b32_e64 v192, v188, v184, s[44:45]
	v_cndmask_b32_e64 v193, v184, v188, s[44:45]
	v_cndmask_b32_e64 v194, v189, v185, s[44:45]
	v_cndmask_b32_e64 v195, v185, v189, s[44:45]
	v_cndmask_b32_e64 v196, v190, v186, s[44:45]
	v_cndmask_b32_e64 v197, v186, v190, s[44:45]
	v_cndmask_b32_e64 v198, v191, v187, s[44:45]
	v_cndmask_b32_e64 v199, v187, v191, s[44:45]
	v_add_f32_dpp v200, v192, v193 quad_perm:[3,2,1,0] row_mask:0xf bank_mask:0xf
	v_add_f32_dpp v201, v194, v195 quad_perm:[3,2,1,0] row_mask:0xf bank_mask:0xf
	v_add_f32_dpp v202, v196, v197 quad_perm:[3,2,1,0] row_mask:0xf bank_mask:0xf
	v_add_f32_dpp v203, v198, v199 quad_perm:[3,2,1,0] row_mask:0xf bank_mask:0xf
	v_cndmask_b32_e64 v204, v202, v200, s[42:43]
	v_cndmask_b32_e64 v205, v200, v202, s[42:43]
	v_cndmask_b32_e64 v206, v203, v201, s[42:43]
	v_cndmask_b32_e64 v207, v201, v203, s[42:43]
	s_nop 0
	v_add_f32_dpp v208, v204, v205 quad_perm:[1,0,3,2] row_mask:0xf bank_mask:0xf
	v_add_f32_dpp v209, v206, v207 quad_perm:[1,0,3,2] row_mask:0xf bank_mask:0xf
	v_cvt_pk_bf16_f32 v210, v208, v209
	s_lshl_b32 s2, s20, 8
	s_add_u32 s2, s34, s2
	s_addc_u32 s3, s35, 0
	global_store_dword v3, v210, s[2:3]
	s_mov_b32 s20, s21
	s_mov_b32 s48, s49
	s_mov_b32 s21, s22
	s_mov_b32 s49, s50
	s_cmp_eq_u32 s48, 0
	s_cbranch_scc1 .Lub_drain
	s_cmp_lg_u32 s26, 32
	s_cbranch_scc1 .Lub_norot_l1
	v_readfirstlane_b32 s23, v6
	s_mov_b64 exec, 1
	global_atomic_inc v6, v5, v7, s[6:7] sc0
	s_mov_b64 exec, -1
	s_mov_b32 s26, 0

.Lub_got_l1:
	s_lshl_b32 s2, s22, 8
	s_add_u32 s2, s28, s2
	s_addc_u32 s3, s29, 0
	global_load_dwordx4 v[16:19], v2, s[2:3]
	global_load_dwordx4 v[20:23], v2, s[2:3] offset:16
	s_lshl_b32 s2, s21, 12
	s_add_u32 s2, s30, s2
	s_addc_u32 s3, s31, 0
	global_load_dwordx4 v[24:27], v4, s[2:3]
	global_load_dwordx4 v[28:31], v4, s[2:3] offset:16
	s_waitcnt vmcnt(20)
	v_cvt_pk_f32_fp8_e32 v[116:117], v48
	v_cvt_pk_f32_fp8_sdwa v[118:119], v48 src0_sel:WORD_1
	v_cvt_pk_f32_fp8_e32 v[120:121], v49
	v_cvt_pk_f32_fp8_sdwa v[122:123], v49 src0_sel:WORD_1
	v_cvt_pk_f32_fp8_e32 v[124:125], v50
	v_cvt_pk_f32_fp8_sdwa v[126:127], v50 src0_sel:WORD_1
	v_cvt_pk_f32_fp8_e32 v[128:129], v51
	v_cvt_pk_f32_fp8_sdwa v[130:131], v51 src0_sel:WORD_1
	v_lshlrev_b32_e32 v148, 16, v32
	v_and_b32_e32 v149, 0xffff0000, v32
	v_lshlrev_b32_e32 v150, 16, v33
	v_and_b32_e32 v151, 0xffff0000, v33
	v_lshlrev_b32_e32 v152, 16, v34
	v_and_b32_e32 v153, 0xffff0000, v34
	v_lshlrev_b32_e32 v154, 16, v35
	v_and_b32_e32 v155, 0xffff0000, v35
	v_lshlrev_b32_e32 v156, 16, v36
	v_and_b32_e32 v157, 0xffff0000, v36
	v_lshlrev_b32_e32 v158, 16, v37
	v_and_b32_e32 v159, 0xffff0000, v37
	v_lshlrev_b32_e32 v160, 16, v38
	v_and_b32_e32 v161, 0xffff0000, v38
	v_lshlrev_b32_e32 v162, 16, v39
	v_and_b32_e32 v163, 0xffff0000, v39
	v_lshlrev_b32_sdwa v112, s47, v8 dst_sel:DWORD dst_unused:UNUSED_PAD src0_sel:DWORD src1_sel:WORD_0
	v_or_b32_e32 v112, v112, v1
	buffer_load_dwordx4 v[48:51], v112, s[36:39], 0 offen
	v_pk_mul_f32 v[164:165], v[116:117], v[148:149]
	v_pk_fma_f32 v[164:165], v[118:119], v[150:151], v[164:165]
	v_pk_fma_f32 v[164:165], v[120:121], v[152:153], v[164:165]
	v_pk_fma_f32 v[164:165], v[122:123], v[154:155], v[164:165]
	v_pk_fma_f32 v[164:165], v[124:125], v[156:157], v[164:165]
	v_pk_fma_f32 v[164:165], v[126:127], v[158:159], v[164:165]
	v_pk_fma_f32 v[164:165], v[128:129], v[160:161], v[164:165]
	v_pk_fma_f32 v[164:165], v[130:131], v[162:163], v[164:165]
	v_add_f32_e32 v168, v164, v165
	s_waitcnt vmcnt(20)
	v_cvt_pk_f32_fp8_e32 v[132:133], v52
	v_cvt_pk_f32_fp8_sdwa v[134:135], v52 src0_sel:WORD_1
	v_cvt_pk_f32_fp8_e32 v[136:137], v53
	v_cvt_pk_f32_fp8_sdwa v[138:139], v53 src0_sel:WORD_1
	v_cvt_pk_f32_fp8_e32 v[140:141], v54
	v_cvt_pk_f32_fp8_sdwa v[142:143], v54 src0_sel:WORD_1
	v_cvt_pk_f32_fp8_e32 v[144:145], v55
	v_cvt_pk_f32_fp8_sdwa v[146:147], v55 src0_sel:WORD_1
	v_lshlrev_b32_sdwa v113, s47, v8 dst_sel:DWORD dst_unused:UNUSED_PAD src0_sel:DWORD src1_sel:WORD_1
	v_or_b32_e32 v113, v113, v1
	buffer_load_dwordx4 v[52:55], v113, s[36:39], 0 offen
	v_pk_mul_f32 v[166:167], v[132:133], v[148:149]
	v_pk_fma_f32 v[166:167], v[134:135], v[150:151], v[166:167]
	v_pk_fma_f32 v[166:167], v[136:137], v[152:153], v[166:167]
	v_pk_fma_f32 v[166:167], v[138:139], v[154:155], v[166:167]
	v_pk_fma_f32 v[166:167], v[140:141], v[156:157], v[166:167]
	v_pk_fma_f32 v[166:167], v[142:143], v[158:159], v[166:167]
	v_pk_fma_f32 v[166:167], v[144:145], v[160:161], v[166:167]
	v_pk_fma_f32 v[166:167], v[146:147], v[162:163], v[166:167]
	v_add_f32_e32 v169, v166, v167
	s_waitcnt vmcnt(20)
	v_cvt_pk_f32_fp8_e32 v[116:117], v56
	v_cvt_pk_f32_fp8_sdwa v[118:119], v56 src0_sel:WORD_1
	v_cvt_pk_f32_fp8_e32 v[120:121], v57
	v_cvt_pk_f32_fp8_sdwa v[122:123], v57 src0_sel:WORD_1
	v_cvt_pk_f32_fp8_e32 v[124:125], v58
	v_cvt_pk_f32_fp8_sdwa v[126:127], v58 src0_sel:WORD_1
	v_cvt_pk_f32_fp8_e32 v[128:129], v59
	v_cvt_pk_f32_fp8_sdwa v[130:131], v59 src0_sel:WORD_1
	v_lshlrev_b32_sdwa v112, s47, v9 dst_sel:DWORD dst_unused:UNUSED_PAD src0_sel:DWORD src1_sel:WORD_0
	v_or_b32_e32 v112, v112, v1
	buffer_load_dwordx4 v[56:59], v112, s[36:39], 0 offen
	v_pk_mul_f32 v[164:165], v[116:117], v[148:149]
	v_pk_fma_f32 v[164:165], v[118:119], v[150:151], v[164:165]
	v_pk_fma_f32 v[164:165], v[120:121], v[152:153], v[164:165]
	v_pk_fma_f32 v[164:165], v[122:123], v[154:155], v[164:165]
	v_pk_fma_f32 v[164:165], v[124:125], v[156:157], v[164:165]
	v_pk_fma_f32 v[164:165], v[126:127], v[158:159], v[164:165]
	v_pk_fma_f32 v[164:165], v[128:129], v[160:161], v[164:165]
	v_pk_fma_f32 v[164:165], v[130:131], v[162:163], v[164:165]
	v_add_f32_e32 v170, v164, v165
	s_waitcnt vmcnt(20)
	v_cvt_pk_f32_fp8_e32 v[132:133], v60
	v_cvt_pk_f32_fp8_sdwa v[134:135], v60 src0_sel:WORD_1
	v_cvt_pk_f32_fp8_e32 v[136:137], v61
	v_cvt_pk_f32_fp8_sdwa v[138:139], v61 src0_sel:WORD_1
	v_cvt_pk_f32_fp8_e32 v[140:141], v62
	v_cvt_pk_f32_fp8_sdwa v[142:143], v62 src0_sel:WORD_1
	v_cvt_pk_f32_fp8_e32 v[144:145], v63
	v_cvt_pk_f32_fp8_sdwa v[146:147], v63 src0_sel:WORD_1
	v_lshlrev_b32_sdwa v113, s47, v9 dst_sel:DWORD dst_unused:UNUSED_PAD src0_sel:DWORD src1_sel:WORD_1
	v_or_b32_e32 v113, v113, v1
	buffer_load_dwordx4 v[60:63], v113, s[36:39], 0 offen
	v_pk_mul_f32 v[166:167], v[132:133], v[148:149]
	v_pk_fma_f32 v[166:167], v[134:135], v[150:151], v[166:167]
	v_pk_fma_f32 v[166:167], v[136:137], v[152:153], v[166:167]
	v_pk_fma_f32 v[166:167], v[138:139], v[154:155], v[166:167]
	v_pk_fma_f32 v[166:167], v[140:141], v[156:157], v[166:167]
	v_pk_fma_f32 v[166:167], v[142:143], v[158:159], v[166:167]
	v_pk_fma_f32 v[166:167], v[144:145], v[160:161], v[166:167]
	v_pk_fma_f32 v[166:167], v[146:147], v[162:163], v[166:167]
	v_add_f32_e32 v171, v166, v167
	s_waitcnt vmcnt(20)
	v_cvt_pk_f32_fp8_e32 v[116:117], v64
	v_cvt_pk_f32_fp8_sdwa v[118:119], v64 src0_sel:WORD_1
	v_cvt_pk_f32_fp8_e32 v[120:121], v65
	v_cvt_pk_f32_fp8_sdwa v[122:123], v65 src0_sel:WORD_1
	v_cvt_pk_f32_fp8_e32 v[124:125], v66
	v_cvt_pk_f32_fp8_sdwa v[126:127], v66 src0_sel:WORD_1
	v_cvt_pk_f32_fp8_e32 v[128:129], v67
	v_cvt_pk_f32_fp8_sdwa v[130:131], v67 src0_sel:WORD_1
	v_lshlrev_b32_sdwa v112, s47, v10 dst_sel:DWORD dst_unused:UNUSED_PAD src0_sel:DWORD src1_sel:WORD_0
	v_or_b32_e32 v112, v112, v1
	buffer_load_dwordx4 v[64:67], v112, s[36:39], 0 offen
	v_pk_mul_f32 v[164:165], v[116:117], v[148:149]
	v_pk_fma_f32 v[164:165], v[118:119], v[150:151], v[164:165]
	v_pk_fma_f32 v[164:165], v[120:121], v[152:153], v[164:165]
	v_pk_fma_f32 v[164:165], v[122:123], v[154:155], v[164:165]
	v_pk_fma_f32 v[164:165], v[124:125], v[156:157], v[164:165]
	v_pk_fma_f32 v[164:165], v[126:127], v[158:159], v[164:165]
	v_pk_fma_f32 v[164:165], v[128:129], v[160:161], v[164:165]
	v_pk_fma_f32 v[164:165], v[130:131], v[162:163], v[164:165]
	v_add_f32_e32 v172, v164, v165
	s_waitcnt vmcnt(20)
	v_cvt_pk_f32_fp8_e32 v[132:133], v68
	v_cvt_pk_f32_fp8_sdwa v[134:135], v68 src0_sel:WORD_1
	v_cvt_pk_f32_fp8_e32 v[136:137], v69
	v_cvt_pk_f32_fp8_sdwa v[138:139], v69 src0_sel:WORD_1
	v_cvt_pk_f32_fp8_e32 v[140:141], v70
	v_cvt_pk_f32_fp8_sdwa v[142:143], v70 src0_sel:WORD_1
	v_cvt_pk_f32_fp8_e32 v[144:145], v71
	v_cvt_pk_f32_fp8_sdwa v[146:147], v71 src0_sel:WORD_1
	v_lshlrev_b32_sdwa v113, s47, v10 dst_sel:DWORD dst_unused:UNUSED_PAD src0_sel:DWORD src1_sel:WORD_1
	v_or_b32_e32 v113, v113, v1
	buffer_load_dwordx4 v[68:71], v113, s[36:39], 0 offen
	v_pk_mul_f32 v[166:167], v[132:133], v[148:149]
	v_pk_fma_f32 v[166:167], v[134:135], v[150:151], v[166:167]
	v_pk_fma_f32 v[166:167], v[136:137], v[152:153], v[166:167]
	v_pk_fma_f32 v[166:167], v[138:139], v[154:155], v[166:167]
	v_pk_fma_f32 v[166:167], v[140:141], v[156:157], v[166:167]
	v_pk_fma_f32 v[166:167], v[142:143], v[158:159], v[166:167]
	v_pk_fma_f32 v[166:167], v[144:145], v[160:161], v[166:167]
	v_pk_fma_f32 v[166:167], v[146:147], v[162:163], v[166:167]
	v_add_f32_e32 v173, v166, v167
	s_waitcnt vmcnt(20)
	v_cvt_pk_f32_fp8_e32 v[116:117], v72
	v_cvt_pk_f32_fp8_sdwa v[118:119], v72 src0_sel:WORD_1
	v_cvt_pk_f32_fp8_e32 v[120:121], v73
	v_cvt_pk_f32_fp8_sdwa v[122:123], v73 src0_sel:WORD_1
	v_cvt_pk_f32_fp8_e32 v[124:125], v74
	v_cvt_pk_f32_fp8_sdwa v[126:127], v74 src0_sel:WORD_1
	v_cvt_pk_f32_fp8_e32 v[128:129], v75
	v_cvt_pk_f32_fp8_sdwa v[130:131], v75 src0_sel:WORD_1
	v_lshlrev_b32_sdwa v112, s47, v11 dst_sel:DWORD dst_unused:UNUSED_PAD src0_sel:DWORD src1_sel:WORD_0
	v_or_b32_e32 v112, v112, v1
	buffer_load_dwordx4 v[72:75], v112, s[36:39], 0 offen
	v_pk_mul_f32 v[164:165], v[116:117], v[148:149]
	v_pk_fma_f32 v[164:165], v[118:119], v[150:151], v[164:165]
	v_pk_fma_f32 v[164:165], v[120:121], v[152:153], v[164:165]
	v_pk_fma_f32 v[164:165], v[122:123], v[154:155], v[164:165]
	v_pk_fma_f32 v[164:165], v[124:125], v[156:157], v[164:165]
	v_pk_fma_f32 v[164:165], v[126:127], v[158:159], v[164:165]
	v_pk_fma_f32 v[164:165], v[128:129], v[160:161], v[164:165]
	v_pk_fma_f32 v[164:165], v[130:131], v[162:163], v[164:165]
	v_add_f32_e32 v174, v164, v165
	s_waitcnt vmcnt(20)
	v_cvt_pk_f32_fp8_e32 v[132:133], v76
	v_cvt_pk_f32_fp8_sdwa v[134:135], v76 src0_sel:WORD_1
	v_cvt_pk_f32_fp8_e32 v[136:137], v77
	v_cvt_pk_f32_fp8_sdwa v[138:139], v77 src0_sel:WORD_1
	v_cvt_pk_f32_fp8_e32 v[140:141], v78
	v_cvt_pk_f32_fp8_sdwa v[142:143], v78 src0_sel:WORD_1
	v_cvt_pk_f32_fp8_e32 v[144:145], v79
	v_cvt_pk_f32_fp8_sdwa v[146:147], v79 src0_sel:WORD_1
	v_lshlrev_b32_sdwa v113, s47, v11 dst_sel:DWORD dst_unused:UNUSED_PAD src0_sel:DWORD src1_sel:WORD_1
	v_or_b32_e32 v113, v113, v1
	buffer_load_dwordx4 v[76:79], v113, s[36:39], 0 offen
	v_pk_mul_f32 v[166:167], v[132:133], v[148:149]
	v_pk_fma_f32 v[166:167], v[134:135], v[150:151], v[166:167]
	v_pk_fma_f32 v[166:167], v[136:137], v[152:153], v[166:167]
	v_pk_fma_f32 v[166:167], v[138:139], v[154:155], v[166:167]
	v_pk_fma_f32 v[166:167], v[140:141], v[156:157], v[166:167]
	v_pk_fma_f32 v[166:167], v[142:143], v[158:159], v[166:167]
	v_pk_fma_f32 v[166:167], v[144:145], v[160:161], v[166:167]
	v_pk_fma_f32 v[166:167], v[146:147], v[162:163], v[166:167]
	v_add_f32_e32 v175, v166, v167
	s_waitcnt vmcnt(20)
	v_cvt_pk_f32_fp8_e32 v[116:117], v80
	v_cvt_pk_f32_fp8_sdwa v[118:119], v80 src0_sel:WORD_1
	v_cvt_pk_f32_fp8_e32 v[120:121], v81
	v_cvt_pk_f32_fp8_sdwa v[122:123], v81 src0_sel:WORD_1
	v_cvt_pk_f32_fp8_e32 v[124:125], v82
	v_cvt_pk_f32_fp8_sdwa v[126:127], v82 src0_sel:WORD_1
	v_cvt_pk_f32_fp8_e32 v[128:129], v83
	v_cvt_pk_f32_fp8_sdwa v[130:131], v83 src0_sel:WORD_1
	v_lshlrev_b32_sdwa v112, s47, v12 dst_sel:DWORD dst_unused:UNUSED_PAD src0_sel:DWORD src1_sel:WORD_0
	v_or_b32_e32 v112, v112, v1
	buffer_load_dwordx4 v[80:83], v112, s[36:39], 0 offen
	v_pk_mul_f32 v[164:165], v[116:117], v[148:149]
	v_pk_fma_f32 v[164:165], v[118:119], v[150:151], v[164:165]
	v_pk_fma_f32 v[164:165], v[120:121], v[152:153], v[164:165]
	v_pk_fma_f32 v[164:165], v[122:123], v[154:155], v[164:165]
	v_pk_fma_f32 v[164:165], v[124:125], v[156:157], v[164:165]
	v_pk_fma_f32 v[164:165], v[126:127], v[158:159], v[164:165]
	v_pk_fma_f32 v[164:165], v[128:129], v[160:161], v[164:165]
	v_pk_fma_f32 v[164:165], v[130:131], v[162:163], v[164:165]
	v_add_f32_e32 v176, v164, v165
	s_waitcnt vmcnt(20)
	v_cvt_pk_f32_fp8_e32 v[132:133], v84
	v_cvt_pk_f32_fp8_sdwa v[134:135], v84 src0_sel:WORD_1
	v_cvt_pk_f32_fp8_e32 v[136:137], v85
	v_cvt_pk_f32_fp8_sdwa v[138:139], v85 src0_sel:WORD_1
	v_cvt_pk_f32_fp8_e32 v[140:141], v86
	v_cvt_pk_f32_fp8_sdwa v[142:143], v86 src0_sel:WORD_1
	v_cvt_pk_f32_fp8_e32 v[144:145], v87
	v_cvt_pk_f32_fp8_sdwa v[146:147], v87 src0_sel:WORD_1
	v_lshlrev_b32_sdwa v113, s47, v12 dst_sel:DWORD dst_unused:UNUSED_PAD src0_sel:DWORD src1_sel:WORD_1
	v_or_b32_e32 v113, v113, v1
	buffer_load_dwordx4 v[84:87], v113, s[36:39], 0 offen
	v_pk_mul_f32 v[166:167], v[132:133], v[148:149]
	v_pk_fma_f32 v[166:167], v[134:135], v[150:151], v[166:167]
	v_pk_fma_f32 v[166:167], v[136:137], v[152:153], v[166:167]
	v_pk_fma_f32 v[166:167], v[138:139], v[154:155], v[166:167]
	v_pk_fma_f32 v[166:167], v[140:141], v[156:157], v[166:167]
	v_pk_fma_f32 v[166:167], v[142:143], v[158:159], v[166:167]
	v_pk_fma_f32 v[166:167], v[144:145], v[160:161], v[166:167]
	v_pk_fma_f32 v[166:167], v[146:147], v[162:163], v[166:167]
	v_add_f32_e32 v177, v166, v167
	s_waitcnt vmcnt(20)
	v_cvt_pk_f32_fp8_e32 v[116:117], v88
	v_cvt_pk_f32_fp8_sdwa v[118:119], v88 src0_sel:WORD_1
	v_cvt_pk_f32_fp8_e32 v[120:121], v89
	v_cvt_pk_f32_fp8_sdwa v[122:123], v89 src0_sel:WORD_1
	v_cvt_pk_f32_fp8_e32 v[124:125], v90
	v_cvt_pk_f32_fp8_sdwa v[126:127], v90 src0_sel:WORD_1
	v_cvt_pk_f32_fp8_e32 v[128:129], v91
	v_cvt_pk_f32_fp8_sdwa v[130:131], v91 src0_sel:WORD_1
	v_lshlrev_b32_sdwa v112, s47, v13 dst_sel:DWORD dst_unused:UNUSED_PAD src0_sel:DWORD src1_sel:WORD_0
	v_or_b32_e32 v112, v112, v1
	buffer_load_dwordx4 v[88:91], v112, s[36:39], 0 offen
	v_pk_mul_f32 v[164:165], v[116:117], v[148:149]
	v_pk_fma_f32 v[164:165], v[118:119], v[150:151], v[164:165]
	v_pk_fma_f32 v[164:165], v[120:121], v[152:153], v[164:165]
	v_pk_fma_f32 v[164:165], v[122:123], v[154:155], v[164:165]
	v_pk_fma_f32 v[164:165], v[124:125], v[156:157], v[164:165]
	v_pk_fma_f32 v[164:165], v[126:127], v[158:159], v[164:165]
	v_pk_fma_f32 v[164:165], v[128:129], v[160:161], v[164:165]
	v_pk_fma_f32 v[164:165], v[130:131], v[162:163], v[164:165]
	v_add_f32_e32 v178, v164, v165
	s_waitcnt vmcnt(20)
	v_cvt_pk_f32_fp8_e32 v[132:133], v92
	v_cvt_pk_f32_fp8_sdwa v[134:135], v92 src0_sel:WORD_1
	v_cvt_pk_f32_fp8_e32 v[136:137], v93
	v_cvt_pk_f32_fp8_sdwa v[138:139], v93 src0_sel:WORD_1
	v_cvt_pk_f32_fp8_e32 v[140:141], v94
	v_cvt_pk_f32_fp8_sdwa v[142:143], v94 src0_sel:WORD_1
	v_cvt_pk_f32_fp8_e32 v[144:145], v95
	v_cvt_pk_f32_fp8_sdwa v[146:147], v95 src0_sel:WORD_1
	v_lshlrev_b32_sdwa v113, s47, v13 dst_sel:DWORD dst_unused:UNUSED_PAD src0_sel:DWORD src1_sel:WORD_1
	v_or_b32_e32 v113, v113, v1
	buffer_load_dwordx4 v[92:95], v113, s[36:39], 0 offen
	v_pk_mul_f32 v[166:167], v[132:133], v[148:149]
	v_pk_fma_f32 v[166:167], v[134:135], v[150:151], v[166:167]
	v_pk_fma_f32 v[166:167], v[136:137], v[152:153], v[166:167]
	v_pk_fma_f32 v[166:167], v[138:139], v[154:155], v[166:167]
	v_pk_fma_f32 v[166:167], v[140:141], v[156:157], v[166:167]
	v_pk_fma_f32 v[166:167], v[142:143], v[158:159], v[166:167]
	v_pk_fma_f32 v[166:167], v[144:145], v[160:161], v[166:167]
	v_pk_fma_f32 v[166:167], v[146:147], v[162:163], v[166:167]
	v_add_f32_e32 v179, v166, v167
	s_waitcnt vmcnt(20)
	v_cvt_pk_f32_fp8_e32 v[116:117], v96
	v_cvt_pk_f32_fp8_sdwa v[118:119], v96 src0_sel:WORD_1
	v_cvt_pk_f32_fp8_e32 v[120:121], v97
	v_cvt_pk_f32_fp8_sdwa v[122:123], v97 src0_sel:WORD_1
	v_cvt_pk_f32_fp8_e32 v[124:125], v98
	v_cvt_pk_f32_fp8_sdwa v[126:127], v98 src0_sel:WORD_1
	v_cvt_pk_f32_fp8_e32 v[128:129], v99
	v_cvt_pk_f32_fp8_sdwa v[130:131], v99 src0_sel:WORD_1
	v_lshlrev_b32_sdwa v112, s47, v14 dst_sel:DWORD dst_unused:UNUSED_PAD src0_sel:DWORD src1_sel:WORD_0
	v_or_b32_e32 v112, v112, v1
	buffer_load_dwordx4 v[96:99], v112, s[36:39], 0 offen
	v_pk_mul_f32 v[164:165], v[116:117], v[148:149]
	v_pk_fma_f32 v[164:165], v[118:119], v[150:151], v[164:165]
	v_pk_fma_f32 v[164:165], v[120:121], v[152:153], v[164:165]
	v_pk_fma_f32 v[164:165], v[122:123], v[154:155], v[164:165]
	v_pk_fma_f32 v[164:165], v[124:125], v[156:157], v[164:165]
	v_pk_fma_f32 v[164:165], v[126:127], v[158:159], v[164:165]
	v_pk_fma_f32 v[164:165], v[128:129], v[160:161], v[164:165]
	v_pk_fma_f32 v[164:165], v[130:131], v[162:163], v[164:165]
	v_add_f32_e32 v180, v164, v165
	s_waitcnt vmcnt(20)
	v_cvt_pk_f32_fp8_e32 v[132:133], v100
	v_cvt_pk_f32_fp8_sdwa v[134:135], v100 src0_sel:WORD_1
	v_cvt_pk_f32_fp8_e32 v[136:137], v101
	v_cvt_pk_f32_fp8_sdwa v[138:139], v101 src0_sel:WORD_1
	v_cvt_pk_f32_fp8_e32 v[140:141], v102
	v_cvt_pk_f32_fp8_sdwa v[142:143], v102 src0_sel:WORD_1
	v_cvt_pk_f32_fp8_e32 v[144:145], v103
	v_cvt_pk_f32_fp8_sdwa v[146:147], v103 src0_sel:WORD_1
	v_lshlrev_b32_sdwa v113, s47, v14 dst_sel:DWORD dst_unused:UNUSED_PAD src0_sel:DWORD src1_sel:WORD_1
	v_or_b32_e32 v113, v113, v1
	buffer_load_dwordx4 v[100:103], v113, s[36:39], 0 offen
	v_pk_mul_f32 v[166:167], v[132:133], v[148:149]
	v_pk_fma_f32 v[166:167], v[134:135], v[150:151], v[166:167]
	v_pk_fma_f32 v[166:167], v[136:137], v[152:153], v[166:167]
	v_pk_fma_f32 v[166:167], v[138:139], v[154:155], v[166:167]
	v_pk_fma_f32 v[166:167], v[140:141], v[156:157], v[166:167]
	v_pk_fma_f32 v[166:167], v[142:143], v[158:159], v[166:167]
	v_pk_fma_f32 v[166:167], v[144:145], v[160:161], v[166:167]
	v_pk_fma_f32 v[166:167], v[146:147], v[162:163], v[166:167]
	v_add_f32_e32 v181, v166, v167
	s_waitcnt vmcnt(20)
	v_cvt_pk_f32_fp8_e32 v[116:117], v104
	v_cvt_pk_f32_fp8_sdwa v[118:119], v104 src0_sel:WORD_1
	v_cvt_pk_f32_fp8_e32 v[120:121], v105
	v_cvt_pk_f32_fp8_sdwa v[122:123], v105 src0_sel:WORD_1
	v_cvt_pk_f32_fp8_e32 v[124:125], v106
	v_cvt_pk_f32_fp8_sdwa v[126:127], v106 src0_sel:WORD_1
	v_cvt_pk_f32_fp8_e32 v[128:129], v107
	v_cvt_pk_f32_fp8_sdwa v[130:131], v107 src0_sel:WORD_1
	v_lshlrev_b32_sdwa v112, s47, v15 dst_sel:DWORD dst_unused:UNUSED_PAD src0_sel:DWORD src1_sel:WORD_0
	v_or_b32_e32 v112, v112, v1
	buffer_load_dwordx4 v[104:107], v112, s[36:39], 0 offen
	v_pk_mul_f32 v[164:165], v[116:117], v[148:149]
	v_pk_fma_f32 v[164:165], v[118:119], v[150:151], v[164:165]
	v_pk_fma_f32 v[164:165], v[120:121], v[152:153], v[164:165]
	v_pk_fma_f32 v[164:165], v[122:123], v[154:155], v[164:165]
	v_pk_fma_f32 v[164:165], v[124:125], v[156:157], v[164:165]
	v_pk_fma_f32 v[164:165], v[126:127], v[158:159], v[164:165]
	v_pk_fma_f32 v[164:165], v[128:129], v[160:161], v[164:165]
	v_pk_fma_f32 v[164:165], v[130:131], v[162:163], v[164:165]
	v_add_f32_e32 v182, v164, v165
	s_waitcnt vmcnt(20)
	v_cvt_pk_f32_fp8_e32 v[132:133], v108
	v_cvt_pk_f32_fp8_sdwa v[134:135], v108 src0_sel:WORD_1
	v_cvt_pk_f32_fp8_e32 v[136:137], v109
	v_cvt_pk_f32_fp8_sdwa v[138:139], v109 src0_sel:WORD_1
	v_cvt_pk_f32_fp8_e32 v[140:141], v110
	v_cvt_pk_f32_fp8_sdwa v[142:143], v110 src0_sel:WORD_1
	v_cvt_pk_f32_fp8_e32 v[144:145], v111
	v_cvt_pk_f32_fp8_sdwa v[146:147], v111 src0_sel:WORD_1
	v_lshlrev_b32_sdwa v113, s47, v15 dst_sel:DWORD dst_unused:UNUSED_PAD src0_sel:DWORD src1_sel:WORD_1
	v_or_b32_e32 v113, v113, v1
	buffer_load_dwordx4 v[108:111], v113, s[36:39], 0 offen
	v_pk_mul_f32 v[166:167], v[132:133], v[148:149]
	v_pk_fma_f32 v[166:167], v[134:135], v[150:151], v[166:167]
	v_pk_fma_f32 v[166:167], v[136:137], v[152:153], v[166:167]
	v_pk_fma_f32 v[166:167], v[138:139], v[154:155], v[166:167]
	v_pk_fma_f32 v[166:167], v[140:141], v[156:157], v[166:167]
	v_pk_fma_f32 v[166:167], v[142:143], v[158:159], v[166:167]
	v_pk_fma_f32 v[166:167], v[144:145], v[160:161], v[166:167]
	v_pk_fma_f32 v[166:167], v[146:147], v[162:163], v[166:167]
	v_add_f32_e32 v183, v166, v167
	s_nop 1
	v_add_f32_dpp v184, v168, v168 row_half_mirror row_mask:0xf bank_mask:0x5
	v_add_f32_dpp v184, v176, v176 row_half_mirror row_mask:0xf bank_mask:0xa
	v_add_f32_dpp v185, v169, v169 row_half_mirror row_mask:0xf bank_mask:0x5
	v_add_f32_dpp v185, v177, v177 row_half_mirror row_mask:0xf bank_mask:0xa
	v_add_f32_dpp v186, v170, v170 row_half_mirror row_mask:0xf bank_mask:0x5
	v_add_f32_dpp v186, v178, v178 row_half_mirror row_mask:0xf bank_mask:0xa
	v_add_f32_dpp v187, v171, v171 row_half_mirror row_mask:0xf bank_mask:0x5
	v_add_f32_dpp v187, v179, v179 row_half_mirror row_mask:0xf bank_mask:0xa
	v_add_f32_dpp v188, v172, v172 row_half_mirror row_mask:0xf bank_mask:0x5
	v_add_f32_dpp v188, v180, v180 row_half_mirror row_mask:0xf bank_mask:0xa
	v_add_f32_dpp v189, v173, v173 row_half_mirror row_mask:0xf bank_mask:0x5
	v_add_f32_dpp v189, v181, v181 row_half_mirror row_mask:0xf bank_mask:0xa
	v_add_f32_dpp v190, v174, v174 row_half_mirror row_mask:0xf bank_mask:0x5
	v_add_f32_dpp v190, v182, v182 row_half_mirror row_mask:0xf bank_mask:0xa
	v_add_f32_dpp v191, v175, v175 row_half_mirror row_mask:0xf bank_mask:0x5
	v_add_f32_dpp v191, v183, v183 row_half_mirror row_mask:0xf bank_mask:0xa
	v_cndmask_b32_e64 v192, v188, v184, s[44:45]
	v_cndmask_b32_e64 v193, v184, v188, s[44:45]
	v_cndmask_b32_e64 v194, v189, v185, s[44:45]
	v_cndmask_b32_e64 v195, v185, v189, s[44:45]
	v_cndmask_b32_e64 v196, v190, v186, s[44:45]
	v_cndmask_b32_e64 v197, v186, v190, s[44:45]
	v_cndmask_b32_e64 v198, v191, v187, s[44:45]
	v_cndmask_b32_e64 v199, v187, v191, s[44:45]
	v_add_f32_dpp v200, v192, v193 quad_perm:[3,2,1,0] row_mask:0xf bank_mask:0xf
	v_add_f32_dpp v201, v194, v195 quad_perm:[3,2,1,0] row_mask:0xf bank_mask:0xf
	v_add_f32_dpp v202, v196, v197 quad_perm:[3,2,1,0] row_mask:0xf bank_mask:0xf
	v_add_f32_dpp v203, v198, v199 quad_perm:[3,2,1,0] row_mask:0xf bank_mask:0xf
	v_cndmask_b32_e64 v204, v202, v200, s[42:43]
	v_cndmask_b32_e64 v205, v200, v202, s[42:43]
	v_cndmask_b32_e64 v206, v203, v201, s[42:43]
	v_cndmask_b32_e64 v207, v201, v203, s[42:43]
	s_nop 0
	v_add_f32_dpp v208, v204, v205 quad_perm:[1,0,3,2] row_mask:0xf bank_mask:0xf
	v_add_f32_dpp v209, v206, v207 quad_perm:[1,0,3,2] row_mask:0xf bank_mask:0xf
	v_cvt_pk_bf16_f32 v210, v208, v209
	s_lshl_b32 s2, s20, 8
	s_add_u32 s2, s34, s2
	s_addc_u32 s3, s35, 0
	global_store_dword v3, v210, s[2:3]
	s_mov_b32 s20, s21
	s_mov_b32 s48, s49
	s_mov_b32 s21, s22
	s_mov_b32 s49, s50
	s_cmp_eq_u32 s48, 0
	s_cbranch_scc1 .Lub_drain
	s_branch .Lub_loop
.Lub_drain:
	s_waitcnt vmcnt(0)
.Lub_next_slice:
	s_waitcnt vmcnt(0)
	s_add_u32 s17, s17, 1
	s_add_u32 s16, s16, 1
	s_cmp_lt_u32 s17, 2
	s_cbranch_scc1 .Lub_slice
